# static s_setprio 1 for waves 0-3 (other half) at the start of P2 and P10; GEMM phases keep their flips
# speedup vs baseline: 1.0015x; 1.0015x over previous
; #define SYNC_AFTER(k) do { if (IN(k) && IN((k) + 1)) { GRID_BAR(); } } while (0)
; __global__ void __launch_bounds__(512, 2) mk_fwd(Params P) {
;     ...
;         pg8::gemm_phase<pg8::EpiProj, pg8::StaticOrder, true, true>(lds, g, S, E);
;     }
;     SYNC_AFTER(1);
;     if (IN(2)) { p2_attention(P, lds, lane, wave, vb); __syncthreads(); p2_mlstm_local(P, lds, tid, lane, wave, vb); }
.Lgb1_t_done:
.Lgb1_exit:
.LBB0_345:
	s_or_b64 exec, exec, s[4:5]
	s_waitcnt lgkmcnt(0)
	s_barrier
	v_readfirstlane_b32 s98, v0
	s_nop 3
	s_lshr_b32 s98, s98, 6
	s_cmp_lt_u32 s98, 4
	s_cbranch_scc0 .Lprio_1
	s_setprio 1
